# L2 prefetch-ahead: each WG touches its 1/32 share of node i+2 W1 (dword per 32B) once per node
# speedup vs baseline: 1.0203x; 1.0018x over previous
.LBB1_2:
	v_lshrrev_b32_e32 v151, 4, v137
	s_lshl_b64 s[6:7], s[2:3], 4
	v_cmp_eq_u32_e64 s[2:3], 1, v151
	s_waitcnt vmcnt(31)
	v_cvt_f16_f32_e32 v8, v8
	v_cmp_gt_u32_e32 vcc, 16, v137
	s_waitcnt vmcnt(29)
	v_cndmask_b32_e64 v116, 0, v116, s[2:3]
	s_waitcnt vmcnt(21)
	v_cndmask_b32_e64 v100, 0, v100, s[2:3]
	v_cmp_eq_u32_e64 s[0:1], 2, v151
	v_cndmask_b32_e64 v114, 0, v114, s[2:3]
	v_cndmask_b32_e64 v115, 0, v115, s[2:3]
	v_cndmask_b32_e32 v6, v116, v6, vcc
	v_cndmask_b32_e64 v116, 0, v117, s[2:3]
	v_cndmask_b32_e64 v108, 0, v108, s[2:3]
	v_cndmask_b32_e32 v26, v100, v26, vcc
	v_cvt_f16_f32_e32 v29, v29
	v_cndmask_b32_e64 v100, 0, v101, s[2:3]
	v_cndmask_b32_e32 v28, 0, v28, vcc
	v_cndmask_b32_e64 v152, 0, 1.0, s[0:1]
	v_cndmask_b32_e32 v114, v114, v120, vcc
	v_cndmask_b32_e32 v115, v115, v121, vcc
	v_cndmask_b32_e32 v7, v116, v7, vcc
	v_cndmask_b32_e64 v106, 0, v106, s[2:3]
	v_cndmask_b32_e64 v107, 0, v107, s[2:3]
	v_cndmask_b32_e32 v14, v108, v14, vcc
	v_cndmask_b32_e64 v108, 0, v109, s[2:3]
	v_cndmask_b32_e32 v27, v100, v27, vcc
	v_cvt_f16_f32_e32 v100, v28
	v_cndmask_b32_e32 v116, 0, v8, vcc
	v_cvt_pk_f16_f32 v8, v6, v7
	v_cvt_pk_f16_f32 v7, v114, v115
	v_cndmask_b32_e64 v114, v152, v140, s[2:3]
	v_cndmask_b32_e32 v106, v106, v112, vcc
	v_cndmask_b32_e32 v107, v107, v113, vcc
	v_cndmask_b32_e32 v15, v108, v15, vcc
	v_cndmask_b32_e64 v98, 0, v98, s[2:3]
	v_cndmask_b32_e64 v99, 0, v99, s[2:3]
	v_cndmask_b32_e32 v110, v114, v110, vcc
	v_cndmask_b32_e64 v114, 0, v141, s[2:3]
	v_cndmask_b32_e32 v108, 0, v16, vcc
	v_cvt_pk_f16_f32 v16, v14, v15
	v_cvt_pk_f16_f32 v15, v106, v107
	v_cndmask_b32_e64 v106, v152, v138, s[2:3]
	v_cndmask_b32_e32 v98, v98, v104, vcc
	v_cndmask_b32_e32 v99, v99, v105, vcc
	v_cndmask_b32_e32 v111, v114, v111, vcc
	v_cndmask_b32_e32 v102, v106, v102, vcc
	v_cndmask_b32_e64 v106, 0, v139, s[2:3]
	v_cndmask_b32_e32 v29, 0, v29, vcc
	v_cvt_pk_f16_f32 v28, v26, v27
	v_cvt_pk_f16_f32 v27, v98, v99
	v_lshlrev_b32_e32 v101, 10, v1
	v_bitop3_b32 v98, v151, v0, 3 bitop3:0x78
	v_lshl_add_u64 v[130:131], s[4:5], 0, v[130:131]
	v_cvt_f16_f32_e32 v4, v4
	v_cvt_pk_f16_f32 v14, v110, v111
	v_cndmask_b32_e32 v103, v106, v103, vcc
	v_pack_b32_f16 v29, v100, v29
	v_lshl_or_b32 v111, v98, 4, v101
	v_lshlrev_b32_e32 v100, 4, v1
	s_movk_i32 s4, 0xc0
	v_cndmask_b32_e64 v124, 0, v124, s[2:3]
	v_cvt_pk_f16_f32 v26, v102, v103
	v_and_b32_e32 v112, 0xc0, v100
	v_bitop3_b32 v100, v100, s4, v111 bitop3:0x26
	s_lshl_b32 s4, s20, 3
	v_lshrrev_b32_e32 v102, 5, v137
	v_lshrrev_b32_e32 v104, 1, v137
	v_cndmask_b32_e64 v122, 0, v122, s[2:3]
	v_cndmask_b32_e64 v123, 0, v123, s[2:3]
	v_cndmask_b32_e32 v2, v124, v2, vcc
	v_cvt_f16_f32_e32 v5, v5
	v_cndmask_b32_e64 v124, 0, v125, s[2:3]
	v_cvt_f16_f32_e32 v9, v9
	v_or_b32_e32 v103, s4, v102
	v_and_or_b32 v110, v104, 8, v101
	v_bitop3_b32 v101, s4, v1, v102 bitop3:0x36
	s_lshl_b32 s4, s20, 4
	v_cndmask_b32_e32 v122, v122, v128, vcc
	v_cndmask_b32_e32 v123, v123, v129, vcc
	v_cndmask_b32_e32 v3, v124, v3, vcc
	v_cndmask_b32_e32 v17, 0, v17, vcc
	v_lshlrev_b32_e32 v107, 4, v101
	v_bitop3_b32 v101, v103, v1, 2 bitop3:0x36
	s_add_i32 s4, s4, 0x10000
	v_bfe_u32 v0, v0, 4, 2
	v_cndmask_b32_e64 v144, v152, v144, s[2:3]
	v_cndmask_b32_e32 v124, 0, v4, vcc
	v_cvt_pk_f16_f32 v4, v2, v3
	v_cvt_pk_f16_f32 v3, v122, v123
	v_cndmask_b32_e64 v122, v152, v142, s[2:3]
	v_cvt_pk_f16_f32 v17, v108, v17
	s_movk_i32 s5, 0x80
	v_lshlrev_b32_e32 v108, 4, v101
	v_bitop3_b32 v101, v103, v1, 4 bitop3:0x36
	s_cmp_lt_u32 s22, 64
	v_lshlrev_b32_e32 v104, 5, v0
	v_lshlrev_b32_e32 v0, 6, v0
	v_cndmask_b32_e32 v126, v144, v126, vcc
	v_cndmask_b32_e64 v144, 0, v145, s[2:3]
	v_cndmask_b32_e32 v118, v122, v118, vcc
	v_cndmask_b32_e64 v122, 0, v143, s[2:3]
	v_bitop3_b32 v99, v112, s5, v111 bitop3:0x36
	v_lshlrev_b32_e32 v109, 4, v101
	v_bitop3_b32 v101, v103, v1, 6 bitop3:0x36
	v_lshl_or_b32 v105, s20, 8, v0
	v_mov_b32_e32 v0, 0x1ec00
	s_cselect_b64 s[4:5], -1, 0
	v_cndmask_b32_e32 v127, v144, v127, vcc
	v_cndmask_b32_e32 v5, 0, v5, vcc
	v_cndmask_b32_e32 v119, v122, v119, vcc
	v_cndmask_b32_e32 v9, 0, v9, vcc
	v_lshlrev_b32_e32 v113, 4, v101
	v_lshlrev_b32_e32 v101, 5, v1
	v_lshl_add_u32 v106, v137, 6, v0
	v_cndmask_b32_e64 v0, 0, 1, s[4:5]
	v_lshl_add_u64 v[132:133], s[8:9], 0, v[132:133]
	v_or_b32_e32 v148, 0x400, v147
	v_or_b32_e32 v149, 0x800, v147
	v_or_b32_e32 v150, 0xc00, v147
	v_cvt_pk_f16_f32 v2, v126, v127
	v_pack_b32_f16 v5, v124, v5
	v_cvt_pk_f16_f32 v6, v118, v119
	v_pack_b32_f16 v9, v116, v9
	v_bitop3_b32 v98, v112, 64, v111 bitop3:0x36
	v_lshl_or_b32 v104, s20, 7, v104
	s_mov_b32 s22, 0x98000
	s_mov_b32 s23, 0x5040100
	s_mov_b32 s24, 0x7060302
	v_add_u32_e32 v107, v107, v110
	v_add_u32_e32 v108, v108, v110
	v_add_u32_e32 v109, v109, v110
	v_add_u32_e32 v110, v113, v110
	v_add_u32_e32 v111, v112, v111
	v_lshlrev_b32_e32 v113, 4, v137
	v_or_b32_e32 v113, 0x10000, v113
	s_lshr_b32 s28, s20, 2
	s_and_b32 s29, s20, 3
	s_lshl_b32 s28, s28, 10
	s_lshl_b32 s29, s29, 2
	s_add_i32 s28, s28, s29
	v_add_u32_e32 v112, s28, v113
	v_cmp_eq_u32_e64 s[26:27], 3, v151
	v_add_u32_e32 v114, 0x12400, v101
	s_lshr_b32 s31, s6, 13
	s_and_b32 s31, s31, 31
	s_lshl_b32 s31, s31, 14
	s_lshl_b32 s33, s20, 11
	s_or_b32 s31, s31, s33
	v_lshl_or_b32 v116, v137, 5, s31
	s_mov_b32 s33, 0x80000
	buffer_load_dword v115, v116, s[16:19], s33 offen
	v_cmp_ne_u32_e64 s[4:5], 1, v0
	v_mov_b32_e32 v121, v136
	v_mov_b32_e32 v144, v136
	v_mov_b32_e32 v0, v136
	v_mov_b32_e32 v1, v136
	s_waitcnt lgkmcnt(0)
	s_barrier
	ds_read_u16 v248, v114
	ds_read_u16 v249, v114 offset:512
	ds_read_u16 v250, v114 offset:1024
	ds_read_u16 v251, v114 offset:1536
	v_add_u32_e32 v114, 2, v114
	s_branch .LBB1_4

.LBB1_4:
	s_waitcnt lgkmcnt(0)
	s_and_saveexec_b64 s[8:9], s[2:3]
	v_cvt_f16_f32_e32 v0, v0
	v_cvt_f16_f32_e32 v1, v1
	v_cvt_f16_f32_e32 v121, v121
	v_cvt_f16_f32_e32 v144, v144
	v_perm_b32 v5, v0, v248, s23
	v_perm_b32 v9, v1, v249, s23
	v_perm_b32 v17, v121, v250, s23
	v_perm_b32 v29, v144, v251, s23
	s_or_b64 exec, exec, s[8:9]
	s_waitcnt vmcnt(17)
	v_cndmask_b32_e64 v0, v30, v134, s[0:1]
	v_bfi_b32 v30, s10, v0, v30
	v_perm_b32 v0, v22, v134, s24
	v_cndmask_b32_e64 v22, v22, v0, s[0:1]
	v_bfi_b32 v1, s10, v135, v18
	v_perm_b32 v0, v10, v135, s24
	v_mfma_f32_16x16x32_f16 v[126:129], v[30:33], v[6:9], 0
	v_cndmask_b32_e64 v18, v18, v1, s[0:1]
	v_cndmask_b32_e64 v10, v10, v0, s[0:1]
	s_cmp_lg_u32 s22, 0x818000
	v_mfma_f32_16x16x32_f16 v[122:125], v[30:33], v[2:5], 0
	s_cselect_b32 s9, s11, 15
	s_nop 2
	v_cvt_pk_f16_f32 v121, v126, v127
	v_cvt_pk_f16_f32 v127, v128, v129
	v_mfma_f32_16x16x32_f16 v[134:137], v[30:33], v[14:17], 0
	v_pk_max_f16 v126, v121, 0
	s_nop 0
	v_cvt_pk_f16_f32 v0, v122, v123
	v_cvt_pk_f16_f32 v1, v124, v125
	v_mfma_f32_16x16x32_f16 v[30:33], v[30:33], v[26:29], 0
	v_pk_max_f16 v127, v127, 0
	v_pk_max_f16 v0, v0, 0
	v_pk_max_f16 v1, v1, 0
	v_mfma_f32_16x16x32_f16 v[122:125], v[22:25], v[2:5], 0
	ds_write2st64_b64 v107, v[0:1], v[126:127] offset1:32
	s_nop 1
	v_cvt_pk_f16_f32 v0, v134, v135
	v_cvt_pk_f16_f32 v1, v136, v137
	v_mfma_f32_16x16x32_f16 v[126:129], v[22:25], v[6:9], 0
	s_nop 0
	v_cvt_pk_f16_f32 v30, v30, v31
	v_cvt_pk_f16_f32 v31, v32, v33
	v_pk_max_f16 v0, v0, 0
	v_mfma_f32_16x16x32_f16 v[134:137], v[22:25], v[14:17], 0
	v_pk_max_f16 v30, v30, 0
	v_pk_max_f16 v31, v31, 0
	v_pk_max_f16 v1, v1, 0
	v_mfma_f32_16x16x32_f16 v[22:25], v[22:25], v[26:29], 0
	ds_write2st64_b64 v107, v[0:1], v[30:31] offset0:64 offset1:96
	v_cvt_pk_f16_f32 v0, v122, v123
	v_cvt_pk_f16_f32 v1, v124, v125
	v_mfma_f32_16x16x32_f16 v[30:33], v[18:21], v[2:5], 0
	v_pk_max_f16 v0, v0, 0
	v_cvt_pk_f16_f32 v139, v128, v129
	v_pk_max_f16 v1, v1, 0
	v_mfma_f32_16x16x32_f16 v[122:125], v[18:21], v[6:9], 0
	v_cvt_pk_f16_f32 v121, v126, v127
	v_pk_max_f16 v138, v121, 0
	v_pk_max_f16 v139, v139, 0
	v_mfma_f32_16x16x32_f16 v[126:129], v[18:21], v[14:17], 0
	ds_write2st64_b64 v108, v[0:1], v[138:139] offset1:32
	v_cvt_pk_f16_f32 v0, v134, v135
	v_cvt_pk_f16_f32 v1, v136, v137
	v_mfma_f32_16x16x32_f16 v[18:21], v[18:21], v[26:29], 0
	v_pk_max_f16 v0, v0, 0
	v_cvt_pk_f16_f32 v139, v24, v25
	v_pk_max_f16 v1, v1, 0
	v_mfma_f32_16x16x32_f16 v[134:137], v[10:13], v[2:5], 0
	v_cvt_pk_f16_f32 v121, v22, v23
	v_pk_max_f16 v138, v121, 0
	v_pk_max_f16 v139, v139, 0
	ds_write2st64_b64 v108, v[0:1], v[138:139] offset0:64 offset1:96
	v_cvt_pk_f16_f32 v0, v30, v31
	v_mfma_f32_16x16x32_f16 v[22:25], v[10:13], v[6:9], 0
	v_cvt_pk_f16_f32 v1, v32, v33
	v_pk_max_f16 v0, v0, 0
	v_cvt_pk_f16_f32 v30, v122, v123
	v_cvt_pk_f16_f32 v31, v124, v125
	v_mfma_f32_16x16x32_f16 v[138:141], v[10:13], v[14:17], 0
	v_pk_max_f16 v1, v1, 0
	v_pk_max_f16 v30, v30, 0
	v_pk_max_f16 v31, v31, 0
	ds_write2st64_b64 v109, v[0:1], v[30:31] offset1:32
	v_cvt_pk_f16_f32 v0, v126, v127
	v_mfma_f32_16x16x32_f16 v[10:13], v[10:13], v[26:29], 0
	v_cvt_pk_f16_f32 v1, v128, v129
	v_pk_max_f16 v0, v0, 0
	v_cvt_pk_f16_f32 v18, v18, v19
	v_cvt_pk_f16_f32 v19, v20, v21
	v_pk_max_f16 v1, v1, 0
	v_pk_max_f16 v18, v18, 0
	v_pk_max_f16 v19, v19, 0
	ds_write2st64_b64 v109, v[0:1], v[18:19] offset0:64 offset1:96
	v_cvt_pk_f16_f32 v0, v134, v135
	v_cvt_pk_f16_f32 v1, v136, v137
	v_pk_max_f16 v0, v0, 0
	v_cvt_pk_f16_f32 v18, v22, v23
	v_cvt_pk_f16_f32 v19, v24, v25
	v_pk_max_f16 v1, v1, 0
	v_pk_max_f16 v18, v18, 0
	v_pk_max_f16 v19, v19, 0
	ds_write2st64_b64 v110, v[0:1], v[18:19] offset1:32
	v_cvt_pk_f16_f32 v0, v138, v139
	v_cvt_pk_f16_f32 v1, v140, v141
	v_pk_max_f16 v0, v0, 0
	v_cvt_pk_f16_f32 v10, v10, v11
	v_cvt_pk_f16_f32 v11, v12, v13
	v_pk_max_f16 v1, v1, 0
	v_pk_max_f16 v10, v10, 0
	v_pk_max_f16 v11, v11, 0
	ds_write2st64_b64 v110, v[0:1], v[10:11] offset0:64 offset1:96
	v_add_u32_e32 v0, 0x12c00, v105
	s_waitcnt lgkmcnt(0)
	s_barrier
	v_add_u32_e32 v1, 0x12c10, v105
	ds_read_b128 v[10:13], v0
	ds_read_b128 v[18:21], v1
	v_add_u32_e32 v0, 0x12c20, v105
	v_add_u32_e32 v1, 0x12c30, v105
	ds_read_b128 v[22:25], v0
	ds_read_b128 v[30:33], v1
	ds_read_b128 v[122:125], v111
	ds_read_b128 v[126:129], v111 offset:16384
	ds_read_b128 v[134:137], v111 offset:32768
	ds_read_b128 v[138:141], v111 offset:49152
	ds_read_b128 v[142:145], v98
	ds_read_b128 v[152:155], v98 offset:16384
	ds_read_b128 v[156:159], v98 offset:32768
	ds_read_b128 v[160:163], v98 offset:49152
	s_lshl_b32 s20, s9, 7
	v_lshl_add_u64 v[0:1], s[20:21], 3, v[132:133]
	s_add_i32 s25, s22, 0xfff88000
	s_lshl_b32 s8, s9, 8
	buffer_load_dwordx4 v[192:195], v147, s[16:19], s25 offen
	buffer_load_dwordx4 v[196:199], v148, s[16:19], s25 offen
	buffer_load_dwordx4 v[200:203], v149, s[16:19], s25 offen
	buffer_load_dwordx4 v[204:207], v150, s[16:19], s25 offen
	s_waitcnt vmcnt(20) lgkmcnt(7)
	v_mfma_f32_16x16x32_f16 v[164:167], v[58:61], v[122:125], v[10:13]
	s_waitcnt lgkmcnt(6)
	v_mfma_f32_16x16x32_f16 v[168:171], v[58:61], v[126:129], v[10:13]
	s_waitcnt lgkmcnt(5)
	v_mfma_f32_16x16x32_f16 v[172:175], v[58:61], v[134:137], v[10:13]
	s_waitcnt lgkmcnt(4)
	v_mfma_f32_16x16x32_f16 v[10:13], v[58:61], v[138:141], v[10:13]
	s_waitcnt vmcnt(19)
	v_mfma_f32_16x16x32_f16 v[58:61], v[54:57], v[122:125], v[18:21]
	v_mfma_f32_16x16x32_f16 v[176:179], v[54:57], v[126:129], v[18:21]
	v_mfma_f32_16x16x32_f16 v[180:183], v[54:57], v[134:137], v[18:21]
	v_mfma_f32_16x16x32_f16 v[18:21], v[54:57], v[138:141], v[18:21]
	s_waitcnt vmcnt(18)
	v_mfma_f32_16x16x32_f16 v[54:57], v[50:53], v[122:125], v[22:25]
	v_mfma_f32_16x16x32_f16 v[184:187], v[50:53], v[126:129], v[22:25]
	v_mfma_f32_16x16x32_f16 v[188:191], v[50:53], v[134:137], v[22:25]
	v_mfma_f32_16x16x32_f16 v[22:25], v[50:53], v[138:141], v[22:25]
	s_waitcnt vmcnt(17)
	v_mfma_f32_16x16x32_f16 v[50:53], v[38:41], v[122:125], v[30:33]
	v_mfma_f32_16x16x32_f16 v[122:125], v[38:41], v[126:129], v[30:33]
	v_mfma_f32_16x16x32_f16 v[126:129], v[38:41], v[134:137], v[30:33]
	v_mfma_f32_16x16x32_f16 v[38:41], v[38:41], v[138:141], v[30:33]
	ds_read_b128 v[136:139], v99
	ds_read_b128 v[208:211], v99 offset:16384
	ds_read_b128 v[212:215], v99 offset:32768
	ds_read_b128 v[216:219], v99 offset:49152
	s_add_i32 s9, s22, 0xfff90000
	s_waitcnt vmcnt(16) lgkmcnt(7)
	v_mfma_f32_16x16x32_f16 v[164:167], v[94:97], v[142:145], v[164:167]
	s_waitcnt lgkmcnt(6)
	v_mfma_f32_16x16x32_f16 v[168:171], v[94:97], v[152:155], v[168:171]
	s_waitcnt vmcnt(15)
	v_mfma_f32_16x16x32_f16 v[58:61], v[90:93], v[142:145], v[58:61]
	v_mfma_f32_16x16x32_f16 v[176:179], v[90:93], v[152:155], v[176:179]
	s_waitcnt vmcnt(14)
	v_mfma_f32_16x16x32_f16 v[54:57], v[78:81], v[142:145], v[54:57]
	v_mfma_f32_16x16x32_f16 v[184:187], v[78:81], v[152:155], v[184:187]
	s_waitcnt vmcnt(13)
	v_mfma_f32_16x16x32_f16 v[50:53], v[34:37], v[142:145], v[50:53]
	buffer_load_dwordx4 v[140:143], v147, s[16:19], s9 offen
	buffer_load_dwordx4 v[220:223], v148, s[16:19], s9 offen
	v_mfma_f32_16x16x32_f16 v[122:125], v[34:37], v[152:155], v[122:125]
	buffer_load_dwordx4 v[152:155], v149, s[16:19], s9 offen
	buffer_load_dwordx4 v[224:227], v150, s[16:19], s9 offen
	s_mov_b32 s9, s21
	s_waitcnt lgkmcnt(5)
	v_mfma_f32_16x16x32_f16 v[172:175], v[94:97], v[156:159], v[172:175]
	s_waitcnt lgkmcnt(4)
	v_mfma_f32_16x16x32_f16 v[94:97], v[94:97], v[160:163], v[10:13]
	s_nop 2
	v_lshl_add_u64 v[10:11], s[8:9], 4, v[130:131]
	v_mfma_f32_16x16x32_f16 v[180:183], v[90:93], v[156:159], v[180:183]
	v_mfma_f32_16x16x32_f16 v[90:93], v[90:93], v[160:163], v[18:21]
	v_mfma_f32_16x16x32_f16 v[188:191], v[78:81], v[156:159], v[188:191]
	v_mfma_f32_16x16x32_f16 v[78:81], v[78:81], v[160:163], v[22:25]
	global_load_dwordx4 v[30:33], v[10:11], off
	s_nop 1
	global_load_dwordx4 v[22:25], v[10:11], off offset:1024
	global_load_dwordx4 v[18:21], v[10:11], off offset:2048
	s_nop 0
	global_load_dwordx4 v[10:13], v[10:11], off offset:3072
	s_nop 0
	global_load_dwordx2 v[134:135], v[0:1], off
	v_mfma_f32_16x16x32_f16 v[126:129], v[34:37], v[156:159], v[126:129]
	v_mfma_f32_16x16x32_f16 v[34:37], v[34:37], v[160:163], v[38:41]
	s_nop 2
	ds_read_b128 v[38:41], v100
	ds_read_b128 v[156:159], v100 offset:16384
	ds_read_b128 v[160:163], v100 offset:32768
	ds_read_b128 v[228:231], v100 offset:49152
	s_add_i32 s8, s22, 0xfff98000
	s_waitcnt vmcnt(21) lgkmcnt(7)
	v_mfma_f32_16x16x32_f16 v[164:167], v[82:85], v[136:139], v[164:167]
	s_waitcnt lgkmcnt(6)
	v_mfma_f32_16x16x32_f16 v[168:171], v[82:85], v[208:211], v[168:171]
	s_waitcnt lgkmcnt(5)
	v_mfma_f32_16x16x32_f16 v[172:175], v[82:85], v[212:215], v[172:175]
	s_waitcnt lgkmcnt(4)
	v_mfma_f32_16x16x32_f16 v[82:85], v[82:85], v[216:219], v[94:97]
	s_waitcnt vmcnt(20)
	v_mfma_f32_16x16x32_f16 v[58:61], v[70:73], v[136:139], v[58:61]
	v_mfma_f32_16x16x32_f16 v[94:97], v[70:73], v[208:211], v[176:179]
	v_mfma_f32_16x16x32_f16 v[176:179], v[70:73], v[212:215], v[180:183]
	v_mfma_f32_16x16x32_f16 v[70:73], v[70:73], v[216:219], v[90:93]
	s_waitcnt vmcnt(19)
	v_mfma_f32_16x16x32_f16 v[54:57], v[62:65], v[136:139], v[54:57]
	v_mfma_f32_16x16x32_f16 v[90:93], v[62:65], v[208:211], v[184:187]
	v_mfma_f32_16x16x32_f16 v[180:183], v[62:65], v[212:215], v[188:191]
	v_mfma_f32_16x16x32_f16 v[62:65], v[62:65], v[216:219], v[78:81]
	s_waitcnt vmcnt(18)
	v_mfma_f32_16x16x32_f16 v[50:53], v[42:45], v[136:139], v[50:53]
	v_mfma_f32_16x16x32_f16 v[78:81], v[42:45], v[208:211], v[122:125]
	v_mfma_f32_16x16x32_f16 v[122:125], v[42:45], v[212:215], v[126:129]
	s_nop 2
	buffer_load_dwordx4 v[126:129], v147, s[16:19], s8 offen
	buffer_load_dwordx4 v[136:139], v148, s[16:19], s8 offen
	buffer_load_dwordx4 v[184:187], v149, s[16:19], s8 offen
	buffer_load_dwordx4 v[188:191], v150, s[16:19], s8 offen
	v_mfma_f32_16x16x32_f16 v[34:37], v[42:45], v[216:219], v[34:37]
	ds_read_b128 v[42:45], v111 offset:256
	ds_read_b128 v[208:211], v111 offset:16640
	ds_read_b128 v[212:215], v111 offset:33024
	ds_read_b128 v[216:219], v111 offset:49408
	s_add_i32 s8, s22, 0xfffa0000
	s_waitcnt vmcnt(21) lgkmcnt(7)
	v_mfma_f32_16x16x32_f16 v[164:167], v[86:89], v[38:41], v[164:167]
	s_waitcnt lgkmcnt(6)
	v_mfma_f32_16x16x32_f16 v[168:171], v[86:89], v[156:159], v[168:171]
	s_waitcnt lgkmcnt(5)
	v_mfma_f32_16x16x32_f16 v[172:175], v[86:89], v[160:163], v[172:175]
	s_waitcnt lgkmcnt(4)
	v_mfma_f32_16x16x32_f16 v[82:85], v[86:89], v[228:231], v[82:85]
	s_waitcnt vmcnt(20)
	v_mfma_f32_16x16x32_f16 v[58:61], v[74:77], v[38:41], v[58:61]
	v_mfma_f32_16x16x32_f16 v[86:89], v[74:77], v[156:159], v[94:97]
	v_mfma_f32_16x16x32_f16 v[94:97], v[74:77], v[160:163], v[176:179]
	v_mfma_f32_16x16x32_f16 v[70:73], v[74:77], v[228:231], v[70:73]
	s_waitcnt vmcnt(19)
	v_mfma_f32_16x16x32_f16 v[54:57], v[66:69], v[38:41], v[54:57]
	v_mfma_f32_16x16x32_f16 v[74:77], v[66:69], v[156:159], v[90:93]
	v_mfma_f32_16x16x32_f16 v[90:93], v[66:69], v[160:163], v[180:183]
	v_mfma_f32_16x16x32_f16 v[62:65], v[66:69], v[228:231], v[62:65]
	s_waitcnt vmcnt(18)
	v_mfma_f32_16x16x32_f16 v[38:41], v[46:49], v[38:41], v[50:53]
	v_mfma_f32_16x16x32_f16 v[50:53], v[46:49], v[156:159], v[78:81]
	v_mfma_f32_16x16x32_f16 v[66:69], v[46:49], v[160:163], v[122:125]
	s_nop 1
	buffer_load_dwordx4 v[78:81], v147, s[16:19], s8 offen
	buffer_load_dwordx4 v[122:125], v148, s[16:19], s8 offen
	buffer_load_dwordx4 v[156:159], v149, s[16:19], s8 offen
	buffer_load_dwordx4 v[160:163], v150, s[16:19], s8 offen
	v_mfma_f32_16x16x32_f16 v[34:37], v[46:49], v[228:231], v[34:37]
	ds_read_b128 v[46:49], v98 offset:256
	ds_read_b128 v[176:179], v98 offset:16640
	ds_read_b128 v[180:183], v98 offset:33024
	ds_read_b128 v[228:231], v98 offset:49408
	s_add_i32 s8, s22, 0xfffa8000
	s_waitcnt vmcnt(20) lgkmcnt(7)
	v_mfma_f32_16x16x32_f16 v[164:167], v[192:195], v[42:45], v[164:167]
	s_waitcnt lgkmcnt(6)
	v_mfma_f32_16x16x32_f16 v[168:171], v[192:195], v[208:211], v[168:171]
	s_waitcnt lgkmcnt(5)
	v_mfma_f32_16x16x32_f16 v[172:175], v[192:195], v[212:215], v[172:175]
	s_waitcnt lgkmcnt(4)
	v_mfma_f32_16x16x32_f16 v[82:85], v[192:195], v[216:219], v[82:85]
	s_waitcnt vmcnt(19)
	v_mfma_f32_16x16x32_f16 v[58:61], v[196:199], v[42:45], v[58:61]
	v_mfma_f32_16x16x32_f16 v[86:89], v[196:199], v[208:211], v[86:89]
	v_mfma_f32_16x16x32_f16 v[94:97], v[196:199], v[212:215], v[94:97]
	v_mfma_f32_16x16x32_f16 v[70:73], v[196:199], v[216:219], v[70:73]
	s_waitcnt vmcnt(18)
	v_mfma_f32_16x16x32_f16 v[54:57], v[200:203], v[42:45], v[54:57]
	v_mfma_f32_16x16x32_f16 v[74:77], v[200:203], v[208:211], v[74:77]
	v_mfma_f32_16x16x32_f16 v[90:93], v[200:203], v[212:215], v[90:93]
	v_mfma_f32_16x16x32_f16 v[62:65], v[200:203], v[216:219], v[62:65]
	s_waitcnt vmcnt(17)
	v_mfma_f32_16x16x32_f16 v[38:41], v[204:207], v[42:45], v[38:41]
	v_mfma_f32_16x16x32_f16 v[42:45], v[204:207], v[208:211], v[50:53]
	v_mfma_f32_16x16x32_f16 v[50:53], v[204:207], v[212:215], v[66:69]
	s_nop 2
	buffer_load_dwordx4 v[66:69], v147, s[16:19], s8 offen
	buffer_load_dwordx4 v[192:195], v148, s[16:19], s8 offen
	buffer_load_dwordx4 v[196:199], v149, s[16:19], s8 offen
	buffer_load_dwordx4 v[200:203], v150, s[16:19], s8 offen
	v_mfma_f32_16x16x32_f16 v[34:37], v[204:207], v[216:219], v[34:37]
	ds_read_b128 v[204:207], v99 offset:256
	ds_read_b128 v[208:211], v99 offset:16640
	ds_read_b128 v[212:215], v99 offset:33024
	ds_read_b128 v[216:219], v99 offset:49408
	s_add_i32 s8, s22, 0xfffb0000
	s_waitcnt vmcnt(20) lgkmcnt(7)
	v_mfma_f32_16x16x32_f16 v[164:167], v[140:143], v[46:49], v[164:167]
	s_waitcnt lgkmcnt(6)
	v_mfma_f32_16x16x32_f16 v[168:171], v[140:143], v[176:179], v[168:171]
	s_waitcnt lgkmcnt(5)
	v_mfma_f32_16x16x32_f16 v[172:175], v[140:143], v[180:183], v[172:175]
	s_waitcnt lgkmcnt(4)
	v_mfma_f32_16x16x32_f16 v[82:85], v[140:143], v[228:231], v[82:85]
	s_waitcnt vmcnt(19)
	v_mfma_f32_16x16x32_f16 v[58:61], v[220:223], v[46:49], v[58:61]
	v_mfma_f32_16x16x32_f16 v[86:89], v[220:223], v[176:179], v[86:89]
	s_waitcnt vmcnt(18)
	v_mfma_f32_16x16x32_f16 v[54:57], v[152:155], v[46:49], v[54:57]
	v_mfma_f32_16x16x32_f16 v[74:77], v[152:155], v[176:179], v[74:77]
	v_mfma_f32_16x16x32_f16 v[90:93], v[152:155], v[180:183], v[90:93]
	v_mfma_f32_16x16x32_f16 v[62:65], v[152:155], v[228:231], v[62:65]
	s_waitcnt vmcnt(17)
	v_mfma_f32_16x16x32_f16 v[38:41], v[224:227], v[46:49], v[38:41]
	v_mfma_f32_16x16x32_f16 v[42:45], v[224:227], v[176:179], v[42:45]
	v_mfma_f32_16x16x32_f16 v[46:49], v[224:227], v[180:183], v[50:53]
	s_nop 2
	buffer_load_dwordx4 v[50:53], v147, s[16:19], s8 offen
	buffer_load_dwordx4 v[140:143], v148, s[16:19], s8 offen
	buffer_load_dwordx4 v[152:155], v149, s[16:19], s8 offen
	buffer_load_dwordx4 v[176:179], v150, s[16:19], s8 offen
	v_mfma_f32_16x16x32_f16 v[94:97], v[220:223], v[180:183], v[94:97]
	v_mfma_f32_16x16x32_f16 v[70:73], v[220:223], v[228:231], v[70:73]
	v_mfma_f32_16x16x32_f16 v[34:37], v[224:227], v[228:231], v[34:37]
	ds_read_b128 v[180:183], v100 offset:256
	ds_read_b128 v[220:223], v100 offset:16640
	ds_read_b128 v[224:227], v100 offset:33024
	ds_read_b128 v[228:231], v100 offset:49408
	s_add_i32 s8, s22, 0xfffb8000
	s_waitcnt vmcnt(15) lgkmcnt(7)
	v_mfma_f32_16x16x32_f16 v[164:167], v[126:129], v[204:207], v[164:167]
	s_waitcnt lgkmcnt(6)
	v_mfma_f32_16x16x32_f16 v[168:171], v[126:129], v[208:211], v[168:171]
	s_waitcnt lgkmcnt(5)
	v_mfma_f32_16x16x32_f16 v[172:175], v[126:129], v[212:215], v[172:175]
	s_waitcnt lgkmcnt(4)
	v_mfma_f32_16x16x32_f16 v[82:85], v[126:129], v[216:219], v[82:85]
	s_waitcnt vmcnt(14)
	v_mfma_f32_16x16x32_f16 v[58:61], v[136:139], v[204:207], v[58:61]
	v_mfma_f32_16x16x32_f16 v[86:89], v[136:139], v[208:211], v[86:89]
	v_mfma_f32_16x16x32_f16 v[94:97], v[136:139], v[212:215], v[94:97]
	v_mfma_f32_16x16x32_f16 v[70:73], v[136:139], v[216:219], v[70:73]
	s_waitcnt vmcnt(13)
	v_mfma_f32_16x16x32_f16 v[54:57], v[184:187], v[204:207], v[54:57]
	v_mfma_f32_16x16x32_f16 v[74:77], v[184:187], v[208:211], v[74:77]
	v_mfma_f32_16x16x32_f16 v[90:93], v[184:187], v[212:215], v[90:93]
	v_mfma_f32_16x16x32_f16 v[62:65], v[184:187], v[216:219], v[62:65]
	s_waitcnt vmcnt(12)
	v_mfma_f32_16x16x32_f16 v[38:41], v[188:191], v[204:207], v[38:41]
	buffer_load_dwordx4 v[126:129], v147, s[16:19], s8 offen
	buffer_load_dwordx4 v[136:139], v148, s[16:19], s8 offen
	buffer_load_dwordx4 v[184:187], v149, s[16:19], s8 offen
	buffer_load_dwordx4 v[204:207], v150, s[16:19], s8 offen
	v_mfma_f32_16x16x32_f16 v[42:45], v[188:191], v[208:211], v[42:45]
	v_mfma_f32_16x16x32_f16 v[46:49], v[188:191], v[212:215], v[46:49]
	v_mfma_f32_16x16x32_f16 v[34:37], v[188:191], v[216:219], v[34:37]
	ds_read_b128 v[188:191], v111 offset:512
	ds_read_b128 v[208:211], v111 offset:16896
	ds_read_b128 v[212:215], v111 offset:33280
	ds_read_b128 v[216:219], v111 offset:49664
	s_add_i32 s8, s22, 0xfffc0000
	s_waitcnt vmcnt(15) lgkmcnt(7)
	v_mfma_f32_16x16x32_f16 v[164:167], v[78:81], v[180:183], v[164:167]
	s_waitcnt lgkmcnt(6)
	v_mfma_f32_16x16x32_f16 v[168:171], v[78:81], v[220:223], v[168:171]
	s_waitcnt lgkmcnt(5)
	v_mfma_f32_16x16x32_f16 v[172:175], v[78:81], v[224:227], v[172:175]
	s_waitcnt lgkmcnt(4)
	v_mfma_f32_16x16x32_f16 v[78:81], v[78:81], v[228:231], v[82:85]
	s_waitcnt vmcnt(14)
	v_mfma_f32_16x16x32_f16 v[58:61], v[122:125], v[180:183], v[58:61]
	v_mfma_f32_16x16x32_f16 v[82:85], v[122:125], v[220:223], v[86:89]
	v_mfma_f32_16x16x32_f16 v[86:89], v[122:125], v[224:227], v[94:97]
	v_mfma_f32_16x16x32_f16 v[70:73], v[122:125], v[228:231], v[70:73]
	s_waitcnt vmcnt(13)
	v_mfma_f32_16x16x32_f16 v[54:57], v[156:159], v[180:183], v[54:57]
	v_mfma_f32_16x16x32_f16 v[74:77], v[156:159], v[220:223], v[74:77]
	v_mfma_f32_16x16x32_f16 v[90:93], v[156:159], v[224:227], v[90:93]
	v_mfma_f32_16x16x32_f16 v[62:65], v[156:159], v[228:231], v[62:65]
	s_waitcnt vmcnt(12)
	v_mfma_f32_16x16x32_f16 v[38:41], v[160:163], v[180:183], v[38:41]
	buffer_load_dwordx4 v[94:97], v147, s[16:19], s8 offen
	buffer_load_dwordx4 v[122:125], v148, s[16:19], s8 offen
	buffer_load_dwordx4 v[156:159], v149, s[16:19], s8 offen
	buffer_load_dwordx4 v[180:183], v150, s[16:19], s8 offen
	v_mfma_f32_16x16x32_f16 v[42:45], v[160:163], v[220:223], v[42:45]
	v_mfma_f32_16x16x32_f16 v[46:49], v[160:163], v[224:227], v[46:49]
	v_mfma_f32_16x16x32_f16 v[34:37], v[160:163], v[228:231], v[34:37]
	ds_read_b128 v[160:163], v98 offset:512
	ds_read_b128 v[220:223], v98 offset:16896
	ds_read_b128 v[224:227], v98 offset:33280
	ds_read_b128 v[228:231], v98 offset:49664
	s_add_i32 s8, s22, 0xfffc8000
	s_waitcnt vmcnt(15) lgkmcnt(7)
	v_mfma_f32_16x16x32_f16 v[164:167], v[66:69], v[188:191], v[164:167]
	s_waitcnt lgkmcnt(6)
	v_mfma_f32_16x16x32_f16 v[168:171], v[66:69], v[208:211], v[168:171]
	s_waitcnt lgkmcnt(5)
	v_mfma_f32_16x16x32_f16 v[172:175], v[66:69], v[212:215], v[172:175]
	s_waitcnt lgkmcnt(4)
	v_mfma_f32_16x16x32_f16 v[66:69], v[66:69], v[216:219], v[78:81]
	s_waitcnt vmcnt(14)
	v_mfma_f32_16x16x32_f16 v[58:61], v[192:195], v[188:191], v[58:61]
	v_mfma_f32_16x16x32_f16 v[78:81], v[192:195], v[208:211], v[82:85]
	v_mfma_f32_16x16x32_f16 v[82:85], v[192:195], v[212:215], v[86:89]
	v_mfma_f32_16x16x32_f16 v[70:73], v[192:195], v[216:219], v[70:73]
	s_waitcnt vmcnt(13)
	v_mfma_f32_16x16x32_f16 v[54:57], v[196:199], v[188:191], v[54:57]
	v_mfma_f32_16x16x32_f16 v[74:77], v[196:199], v[208:211], v[74:77]
	v_mfma_f32_16x16x32_f16 v[86:89], v[196:199], v[212:215], v[90:93]
	v_mfma_f32_16x16x32_f16 v[62:65], v[196:199], v[216:219], v[62:65]
	s_waitcnt vmcnt(12)
	v_mfma_f32_16x16x32_f16 v[38:41], v[200:203], v[188:191], v[38:41]
	buffer_load_dwordx4 v[90:93], v147, s[16:19], s8 offen
	buffer_load_dwordx4 v[188:191], v148, s[16:19], s8 offen
	buffer_load_dwordx4 v[192:195], v149, s[16:19], s8 offen
	buffer_load_dwordx4 v[196:199], v150, s[16:19], s8 offen
	v_mfma_f32_16x16x32_f16 v[42:45], v[200:203], v[208:211], v[42:45]
	v_mfma_f32_16x16x32_f16 v[46:49], v[200:203], v[212:215], v[46:49]
	v_mfma_f32_16x16x32_f16 v[34:37], v[200:203], v[216:219], v[34:37]
	ds_read_b128 v[200:203], v99 offset:512
	ds_read_b128 v[208:211], v99 offset:16896
	ds_read_b128 v[212:215], v99 offset:33280
	ds_read_b128 v[216:219], v99 offset:49664
	s_add_i32 s8, s22, 0xfffd0000
	s_waitcnt vmcnt(15) lgkmcnt(7)
	v_mfma_f32_16x16x32_f16 v[164:167], v[50:53], v[160:163], v[164:167]
	s_waitcnt lgkmcnt(6)
	v_mfma_f32_16x16x32_f16 v[168:171], v[50:53], v[220:223], v[168:171]
	s_waitcnt lgkmcnt(5)
	v_mfma_f32_16x16x32_f16 v[172:175], v[50:53], v[224:227], v[172:175]
	s_waitcnt lgkmcnt(4)
	v_mfma_f32_16x16x32_f16 v[50:53], v[50:53], v[228:231], v[66:69]
	s_waitcnt vmcnt(14)
	v_mfma_f32_16x16x32_f16 v[58:61], v[140:143], v[160:163], v[58:61]
	v_mfma_f32_16x16x32_f16 v[66:69], v[140:143], v[220:223], v[78:81]
	v_mfma_f32_16x16x32_f16 v[78:81], v[140:143], v[224:227], v[82:85]
	v_mfma_f32_16x16x32_f16 v[70:73], v[140:143], v[228:231], v[70:73]
	s_waitcnt vmcnt(13)
	v_mfma_f32_16x16x32_f16 v[54:57], v[152:155], v[160:163], v[54:57]
	v_mfma_f32_16x16x32_f16 v[74:77], v[152:155], v[220:223], v[74:77]
	v_mfma_f32_16x16x32_f16 v[82:85], v[152:155], v[224:227], v[86:89]
	v_mfma_f32_16x16x32_f16 v[62:65], v[152:155], v[228:231], v[62:65]
	s_waitcnt vmcnt(12)
	v_mfma_f32_16x16x32_f16 v[38:41], v[176:179], v[160:163], v[38:41]
	buffer_load_dwordx4 v[86:89], v147, s[16:19], s8 offen
	buffer_load_dwordx4 v[140:143], v148, s[16:19], s8 offen
	buffer_load_dwordx4 v[152:155], v149, s[16:19], s8 offen
	buffer_load_dwordx4 v[160:163], v150, s[16:19], s8 offen
	v_mfma_f32_16x16x32_f16 v[42:45], v[176:179], v[220:223], v[42:45]
	v_mfma_f32_16x16x32_f16 v[46:49], v[176:179], v[224:227], v[46:49]
	v_mfma_f32_16x16x32_f16 v[34:37], v[176:179], v[228:231], v[34:37]
	ds_read_b128 v[176:179], v100 offset:512
	ds_read_b128 v[220:223], v100 offset:16896
	ds_read_b128 v[224:227], v100 offset:33280
	ds_read_b128 v[228:231], v100 offset:49664
	s_add_i32 s8, s22, 0xfffd8000
	s_waitcnt vmcnt(15) lgkmcnt(7)
	v_mfma_f32_16x16x32_f16 v[164:167], v[126:129], v[200:203], v[164:167]
	s_waitcnt lgkmcnt(6)
	v_mfma_f32_16x16x32_f16 v[168:171], v[126:129], v[208:211], v[168:171]
	s_waitcnt lgkmcnt(5)
	v_mfma_f32_16x16x32_f16 v[172:175], v[126:129], v[212:215], v[172:175]
	s_waitcnt lgkmcnt(4)
	v_mfma_f32_16x16x32_f16 v[50:53], v[126:129], v[216:219], v[50:53]
	s_waitcnt vmcnt(14)
	v_mfma_f32_16x16x32_f16 v[58:61], v[136:139], v[200:203], v[58:61]
	v_mfma_f32_16x16x32_f16 v[66:69], v[136:139], v[208:211], v[66:69]
	v_mfma_f32_16x16x32_f16 v[78:81], v[136:139], v[212:215], v[78:81]
	v_mfma_f32_16x16x32_f16 v[70:73], v[136:139], v[216:219], v[70:73]
	s_waitcnt vmcnt(13)
	v_mfma_f32_16x16x32_f16 v[54:57], v[184:187], v[200:203], v[54:57]
	v_mfma_f32_16x16x32_f16 v[74:77], v[184:187], v[208:211], v[74:77]
	v_mfma_f32_16x16x32_f16 v[82:85], v[184:187], v[212:215], v[82:85]
	v_mfma_f32_16x16x32_f16 v[62:65], v[184:187], v[216:219], v[62:65]
	s_waitcnt vmcnt(12)
	v_mfma_f32_16x16x32_f16 v[38:41], v[204:207], v[200:203], v[38:41]
	buffer_load_dwordx4 v[126:129], v147, s[16:19], s8 offen
	buffer_load_dwordx4 v[136:139], v148, s[16:19], s8 offen
	buffer_load_dwordx4 v[184:187], v149, s[16:19], s8 offen
	buffer_load_dwordx4 v[200:203], v150, s[16:19], s8 offen
	v_mfma_f32_16x16x32_f16 v[42:45], v[204:207], v[208:211], v[42:45]
	v_mfma_f32_16x16x32_f16 v[46:49], v[204:207], v[212:215], v[46:49]
	v_mfma_f32_16x16x32_f16 v[34:37], v[204:207], v[216:219], v[34:37]
	ds_read_b128 v[204:207], v111 offset:768
	ds_read_b128 v[208:211], v111 offset:17152
	ds_read_b128 v[212:215], v111 offset:33536
	ds_read_b128 v[216:219], v111 offset:49920
	s_add_i32 s8, s22, 0xfffe0000
	s_waitcnt vmcnt(15) lgkmcnt(7)
	v_mfma_f32_16x16x32_f16 v[164:167], v[94:97], v[176:179], v[164:167]
	s_waitcnt lgkmcnt(6)
	v_mfma_f32_16x16x32_f16 v[168:171], v[94:97], v[220:223], v[168:171]
	s_waitcnt vmcnt(14)
	v_mfma_f32_16x16x32_f16 v[58:61], v[122:125], v[176:179], v[58:61]
	v_mfma_f32_16x16x32_f16 v[66:69], v[122:125], v[220:223], v[66:69]
	s_waitcnt lgkmcnt(5)
	v_mfma_f32_16x16x32_f16 v[78:81], v[122:125], v[224:227], v[78:81]
	s_waitcnt lgkmcnt(4)
	v_mfma_f32_16x16x32_f16 v[70:73], v[122:125], v[228:231], v[70:73]
	s_waitcnt vmcnt(13)
	v_mfma_f32_16x16x32_f16 v[54:57], v[156:159], v[176:179], v[54:57]
	v_mfma_f32_16x16x32_f16 v[74:77], v[156:159], v[220:223], v[74:77]
	v_mfma_f32_16x16x32_f16 v[82:85], v[156:159], v[224:227], v[82:85]
	v_mfma_f32_16x16x32_f16 v[62:65], v[156:159], v[228:231], v[62:65]
	s_waitcnt vmcnt(12)
	v_mfma_f32_16x16x32_f16 v[38:41], v[180:183], v[176:179], v[38:41]
	v_mfma_f32_16x16x32_f16 v[42:45], v[180:183], v[220:223], v[42:45]
	buffer_load_dwordx4 v[122:125], v147, s[16:19], s8 offen
	buffer_load_dwordx4 v[156:159], v148, s[16:19], s8 offen
	buffer_load_dwordx4 v[176:179], v149, s[16:19], s8 offen
	buffer_load_dwordx4 v[220:223], v150, s[16:19], s8 offen
	v_mfma_f32_16x16x32_f16 v[50:53], v[94:97], v[228:231], v[50:53]
	v_mfma_f32_16x16x32_f16 v[46:49], v[180:183], v[224:227], v[46:49]
	v_mfma_f32_16x16x32_f16 v[34:37], v[180:183], v[228:231], v[34:37]
	v_mfma_f32_16x16x32_f16 v[172:175], v[94:97], v[224:227], v[172:175]
	ds_read_b128 v[94:97], v98 offset:768
	ds_read_b128 v[180:183], v98 offset:17152
	ds_read_b128 v[224:227], v98 offset:33536
	ds_read_b128 v[228:231], v98 offset:49920
	s_add_i32 s8, s22, 0xfffe8000
	s_waitcnt vmcnt(15) lgkmcnt(7)
	v_mfma_f32_16x16x32_f16 v[164:167], v[90:93], v[204:207], v[164:167]
	s_waitcnt lgkmcnt(6)
	v_mfma_f32_16x16x32_f16 v[168:171], v[90:93], v[208:211], v[168:171]
	s_waitcnt lgkmcnt(5)
	v_mfma_f32_16x16x32_f16 v[172:175], v[90:93], v[212:215], v[172:175]
	s_waitcnt lgkmcnt(4)
	v_mfma_f32_16x16x32_f16 v[90:93], v[90:93], v[216:219], v[50:53]
	s_waitcnt vmcnt(14)
	v_mfma_f32_16x16x32_f16 v[232:235], v[188:191], v[204:207], v[58:61]
	v_mfma_f32_16x16x32_f16 v[66:69], v[188:191], v[208:211], v[66:69]
	v_mfma_f32_16x16x32_f16 v[78:81], v[188:191], v[212:215], v[78:81]
	v_mfma_f32_16x16x32_f16 v[70:73], v[188:191], v[216:219], v[70:73]
	s_waitcnt vmcnt(13)
	v_mfma_f32_16x16x32_f16 v[188:191], v[192:195], v[204:207], v[54:57]
	v_mfma_f32_16x16x32_f16 v[74:77], v[192:195], v[208:211], v[74:77]
	v_mfma_f32_16x16x32_f16 v[82:85], v[192:195], v[212:215], v[82:85]
	v_mfma_f32_16x16x32_f16 v[62:65], v[192:195], v[216:219], v[62:65]
	s_waitcnt vmcnt(12)
	v_mfma_f32_16x16x32_f16 v[192:195], v[196:199], v[204:207], v[38:41]
	buffer_load_dwordx4 v[58:61], v147, s[16:19], s8 offen
	buffer_load_dwordx4 v[54:57], v148, s[16:19], s8 offen
	buffer_load_dwordx4 v[50:53], v149, s[16:19], s8 offen
	buffer_load_dwordx4 v[38:41], v150, s[16:19], s8 offen
	v_mfma_f32_16x16x32_f16 v[42:45], v[196:199], v[208:211], v[42:45]
	v_mfma_f32_16x16x32_f16 v[46:49], v[196:199], v[212:215], v[46:49]
	v_mfma_f32_16x16x32_f16 v[196:199], v[196:199], v[216:219], v[34:37]
	ds_read_b128 v[204:207], v99 offset:768
	ds_read_b128 v[208:211], v99 offset:17152
	ds_read_b128 v[212:215], v99 offset:33536
	ds_read_b128 v[216:219], v99 offset:49920
	s_add_i32 s8, s22, 0xffff0000
	s_waitcnt vmcnt(15) lgkmcnt(7)
	v_mfma_f32_16x16x32_f16 v[164:167], v[86:89], v[94:97], v[164:167]
	s_waitcnt lgkmcnt(6)
	v_mfma_f32_16x16x32_f16 v[168:171], v[86:89], v[180:183], v[168:171]
	s_waitcnt lgkmcnt(5)
	v_mfma_f32_16x16x32_f16 v[172:175], v[86:89], v[224:227], v[172:175]
	s_waitcnt lgkmcnt(4)
	v_mfma_f32_16x16x32_f16 v[86:89], v[86:89], v[228:231], v[90:93]
	s_waitcnt vmcnt(14)
	v_mfma_f32_16x16x32_f16 v[232:235], v[140:143], v[94:97], v[232:235]
	v_mfma_f32_16x16x32_f16 v[66:69], v[140:143], v[180:183], v[66:69]
	v_mfma_f32_16x16x32_f16 v[236:239], v[140:143], v[224:227], v[78:81]
	v_mfma_f32_16x16x32_f16 v[70:73], v[140:143], v[228:231], v[70:73]
	s_waitcnt vmcnt(13)
	v_mfma_f32_16x16x32_f16 v[140:143], v[152:155], v[94:97], v[188:191]
	v_mfma_f32_16x16x32_f16 v[74:77], v[152:155], v[180:183], v[74:77]
	v_mfma_f32_16x16x32_f16 v[82:85], v[152:155], v[224:227], v[82:85]
	v_mfma_f32_16x16x32_f16 v[62:65], v[152:155], v[228:231], v[62:65]
	s_waitcnt vmcnt(12)
	v_mfma_f32_16x16x32_f16 v[152:155], v[160:163], v[94:97], v[192:195]
	buffer_load_dwordx4 v[94:97], v147, s[16:19], s8 offen
	buffer_load_dwordx4 v[90:93], v148, s[16:19], s8 offen
	buffer_load_dwordx4 v[78:81], v149, s[16:19], s8 offen
	buffer_load_dwordx4 v[34:37], v150, s[16:19], s8 offen
	v_mfma_f32_16x16x32_f16 v[42:45], v[160:163], v[180:183], v[42:45]
	v_mfma_f32_16x16x32_f16 v[46:49], v[160:163], v[224:227], v[46:49]
	v_mfma_f32_16x16x32_f16 v[160:163], v[160:163], v[228:231], v[196:199]
	ds_read_b128 v[180:183], v100 offset:768
	ds_read_b128 v[188:191], v100 offset:17152
	ds_read_b128 v[192:195], v100 offset:33536
	ds_read_b128 v[196:199], v100 offset:49920
	s_add_i32 s8, s22, 0xffff8000
	s_waitcnt vmcnt(15) lgkmcnt(7)
	v_mfma_f32_16x16x32_f16 v[164:167], v[126:129], v[204:207], v[164:167]
	s_waitcnt lgkmcnt(6)
	v_mfma_f32_16x16x32_f16 v[168:171], v[126:129], v[208:211], v[168:171]
	s_waitcnt lgkmcnt(5)
	v_mfma_f32_16x16x32_f16 v[172:175], v[126:129], v[212:215], v[172:175]
	s_waitcnt lgkmcnt(4)
	v_mfma_f32_16x16x32_f16 v[86:89], v[126:129], v[216:219], v[86:89]
	s_waitcnt vmcnt(14)
	v_mfma_f32_16x16x32_f16 v[126:129], v[136:139], v[204:207], v[232:235]
	v_mfma_f32_16x16x32_f16 v[66:69], v[136:139], v[208:211], v[66:69]
	v_mfma_f32_16x16x32_f16 v[224:227], v[136:139], v[212:215], v[236:239]
	v_mfma_f32_16x16x32_f16 v[136:139], v[136:139], v[216:219], v[70:73]
	s_waitcnt vmcnt(13)
	v_mfma_f32_16x16x32_f16 v[140:143], v[184:187], v[204:207], v[140:143]
	v_mfma_f32_16x16x32_f16 v[74:77], v[184:187], v[208:211], v[74:77]
	v_mfma_f32_16x16x32_f16 v[228:231], v[184:187], v[212:215], v[82:85]
	v_mfma_f32_16x16x32_f16 v[184:187], v[184:187], v[216:219], v[62:65]
	s_waitcnt vmcnt(12)
	v_mfma_f32_16x16x32_f16 v[152:155], v[200:203], v[204:207], v[152:155]
	v_mfma_f32_16x16x32_f16 v[204:207], v[200:203], v[208:211], v[42:45]
	buffer_load_dwordx4 v[82:85], v147, s[16:19], s8 offen
	buffer_load_dwordx4 v[70:73], v148, s[16:19], s8 offen
	buffer_load_dwordx4 v[62:65], v149, s[16:19], s8 offen
	buffer_load_dwordx4 v[42:45], v150, s[16:19], s8 offen
	v_mfma_f32_16x16x32_f16 v[46:49], v[200:203], v[212:215], v[46:49]
	v_mfma_f32_16x16x32_f16 v[160:163], v[200:203], v[216:219], v[160:163]
	v_add_u32_e32 v0, 0x1ac00, v104
	ds_read_b128 v[240:243], v0
	ds_read_b128 v[244:247], v0 offset:16
	s_waitcnt vmcnt(12) lgkmcnt(5)
	v_mfma_f32_16x16x32_f16 v[164:167], v[122:125], v[180:183], v[164:167]
	v_mfma_f32_16x16x32_f16 v[126:129], v[156:159], v[180:183], v[126:129]
	v_mfma_f32_16x16x32_f16 v[140:143], v[176:179], v[180:183], v[140:143]
	v_mfma_f32_16x16x32_f16 v[152:155], v[220:223], v[180:183], v[152:155]
	s_waitcnt lgkmcnt(4)
	v_mfma_f32_16x16x32_f16 v[168:171], v[122:125], v[188:191], v[168:171]
	v_mfma_f32_16x16x32_f16 v[208:211], v[156:159], v[188:191], v[66:69]
	v_mfma_f32_16x16x32_f16 v[212:215], v[176:179], v[188:191], v[74:77]
	v_mfma_f32_16x16x32_f16 v[204:207], v[220:223], v[188:191], v[204:207]
	s_waitcnt lgkmcnt(3)
	v_mfma_f32_16x16x32_f16 v[172:175], v[122:125], v[192:195], v[172:175]
	v_cvt_pk_f16_f32 v232, v164, v165
	v_cvt_pk_f16_f32 v233, v166, v167
	v_pk_max_f16 v232, v232, 0
	v_pk_max_f16 v233, v233, 0
	v_mfma_f32_16x16x32_f16 v[224:227], v[156:159], v[192:195], v[224:227]
	v_cvt_pk_f16_f32 v234, v126, v127
	v_cvt_pk_f16_f32 v235, v128, v129
	v_pk_max_f16 v234, v234, 0
	v_pk_max_f16 v235, v235, 0
	v_mfma_f32_16x16x32_f16 v[228:231], v[176:179], v[192:195], v[228:231]
	v_cvt_pk_f16_f32 v236, v140, v141
	v_cvt_pk_f16_f32 v237, v142, v143
	v_pk_max_f16 v236, v236, 0
	v_pk_max_f16 v237, v237, 0
	v_mfma_f32_16x16x32_f16 v[216:219], v[220:223], v[192:195], v[46:49]
	v_cvt_pk_f16_f32 v238, v152, v153
	v_cvt_pk_f16_f32 v239, v154, v155
	v_pk_max_f16 v238, v238, 0
	v_pk_max_f16 v239, v239, 0
	s_waitcnt lgkmcnt(2)
	v_mfma_f32_16x16x32_f16 v[200:203], v[122:125], v[196:199], v[86:89]
	v_cvt_pk_f16_f32 v180, v168, v169
	v_cvt_pk_f16_f32 v181, v170, v171
	v_pk_max_f16 v180, v180, 0
	v_pk_max_f16 v181, v181, 0
	buffer_load_dwordx4 v[86:89], v147, s[16:19], s22 offen
	buffer_load_dwordx4 v[74:77], v148, s[16:19], s22 offen
	buffer_load_dwordx4 v[66:69], v149, s[16:19], s22 offen
	buffer_load_dwordx4 v[46:49], v150, s[16:19], s22 offen
	v_mfma_f32_16x16x32_f16 v[136:139], v[156:159], v[196:199], v[136:139]
	v_cvt_pk_f16_f32 v182, v208, v209
	v_cvt_pk_f16_f32 v183, v210, v211
	v_pk_max_f16 v182, v182, 0
	v_pk_max_f16 v183, v183, 0
	s_waitcnt lgkmcnt(1)
	v_mfma_f32_16x16x32_f16 v[252:255], v[240:243], v[232:235], 0
	v_mfma_f32_16x16x32_f16 v[184:187], v[176:179], v[196:199], v[184:187]
	v_cvt_pk_f16_f32 v188, v212, v213
	v_cvt_pk_f16_f32 v189, v214, v215
	v_pk_max_f16 v188, v188, 0
	v_pk_max_f16 v189, v189, 0
	s_waitcnt lgkmcnt(0)
	v_mfma_f32_16x16x32_f16 v[252:255], v[244:247], v[236:239], v[252:255]
	v_mfma_f32_16x16x32_f16 v[160:163], v[220:223], v[196:199], v[160:163]
	v_cvt_pk_f16_f32 v190, v204, v205
	v_cvt_pk_f16_f32 v191, v206, v207
	v_pk_max_f16 v190, v190, 0
	v_pk_max_f16 v191, v191, 0
	v_cvt_pk_f16_f32 v232, v172, v173
	v_cvt_pk_f16_f32 v233, v174, v175
	v_pk_max_f16 v232, v232, 0
	v_pk_max_f16 v233, v233, 0
	v_cvt_pk_f16_f32 v234, v224, v225
	v_cvt_pk_f16_f32 v235, v226, v227
	v_pk_max_f16 v234, v234, 0
	v_pk_max_f16 v235, v235, 0
	v_mfma_f32_16x16x32_f16 v[192:195], v[240:243], v[180:183], 0
	v_cvt_pk_f16_f32 v236, v228, v229
	v_cvt_pk_f16_f32 v237, v230, v231
	v_pk_max_f16 v236, v236, 0
	v_pk_max_f16 v237, v237, 0
	v_mfma_f32_16x16x32_f16 v[192:195], v[244:247], v[188:191], v[192:195]
	v_cvt_pk_f16_f32 v238, v216, v217
	v_cvt_pk_f16_f32 v239, v218, v219
	v_pk_max_f16 v238, v238, 0
	v_pk_max_f16 v239, v239, 0
	v_cvt_pk_f16_f32 v180, v200, v201
	v_cvt_pk_f16_f32 v181, v202, v203
	v_pk_max_f16 v180, v180, 0
	v_pk_max_f16 v181, v181, 0
	v_mfma_f32_16x16x32_f16 v[196:199], v[240:243], v[232:235], 0
	v_cvt_pk_f16_f32 v182, v136, v137
	v_cvt_pk_f16_f32 v183, v138, v139
	v_pk_max_f16 v182, v182, 0
	v_pk_max_f16 v183, v183, 0
	v_mfma_f32_16x16x32_f16 v[196:199], v[244:247], v[236:239], v[196:199]
	v_cvt_pk_f16_f32 v188, v184, v185
	v_cvt_pk_f16_f32 v189, v186, v187
	v_pk_max_f16 v188, v188, 0
	v_pk_max_f16 v189, v189, 0
	v_cvt_pk_f16_f32 v190, v160, v161
	v_cvt_pk_f16_f32 v191, v162, v163
	v_pk_max_f16 v190, v190, 0
	v_pk_max_f16 v191, v191, 0
	v_mfma_f32_16x16x32_f16 v[122:125], v[240:243], v[180:183], 0
	s_nop 0
	v_mfma_f32_16x16x32_f16 v[122:125], v[244:247], v[188:191], v[122:125]
	s_load_dword s30, s[12:13], 0x0
	v_cndmask_b32_e64 v0, v252, v192, s[2:3]
	v_cndmask_b32_e64 v0, v0, v196, s[0:1]
	s_nop 4
	v_cndmask_b32_e64 v0, v0, v122, s[26:27]
	ds_write_b32 v112, v0
	s_waitcnt lgkmcnt(0)
	s_barrier
	ds_read_b128 v[232:235], v113
	s_add_i32 s31, s22, 0x68000
	buffer_load_dword v115, v116, s[16:19], s31 offen
	ds_read_b128 v[236:239], v113 offset:1024
	ds_read_u16 v248, v114
	ds_read_u16 v249, v114 offset:512
	ds_read_u16 v250, v114 offset:1024
	ds_read_u16 v251, v114 offset:1536
	s_and_b64 vcc, exec, s[4:5]
	s_waitcnt lgkmcnt(4)
	v_add_f32_e32 v0, v232, v233
	v_add_f32_e32 v1, v234, v235
	v_add_f32_e32 v121, v236, v237
	v_add_f32_e32 v144, v238, v239
	v_add_f32_e32 v0, v0, v1
	v_add_f32_e32 v121, v121, v144
	v_add_f32_e32 v0, v0, v121
	v_add_f32_e32 v0, s30, v0
	s_cbranch_vccnz .Lskip_out
	ds_write_b32 v106, v0
